# baseline (speedup 1.0000x reference)
.Lp_main:
	s_load_dwordx2 s[10:11], s[0:1], 0x0
	s_load_dwordx4 s[12:15], s[0:1], 0x10
	s_load_dwordx2 s[16:17], s[0:1], 0x20
	s_load_dwordx4 s[20:23], s[0:1], 0x28
	v_readfirstlane_b32 s3, v0
	v_and_b32_e32 v154, 63, v0
	v_lshrrev_b32_e32 v155, 5, v154
	v_lshlrev_b32_e32 v156, 4, v0
	v_lshlrev_b32_e32 v157, 4, v154
	v_lshlrev_b32_e32 v158, 8, v1
	v_lshl_add_u32 v158, v155, 5, v158
	v_lshlrev_b32_e32 v159, 4, v155
	v_lshrrev_b32_e32 v160, 3, v0
	v_lshlrev_b32_e32 v160, 12, v160
	v_and_b32_e32 v161, 7, v0
	v_lshl_add_u32 v160, v161, 4, v160
	s_lshr_b32 s41, s2, 3
	s_and_b32 s42, s2, 7
	s_lshl_b32 s24, s42, 2
	s_bfe_u32 s25, s2, 0x20003
	s_add_u32 s24, s24, s25
	s_lshr_b32 s25, s2, 5
	s_lshr_b32 s26, s3, 6
	s_lshl_b32 s27, s25, 2
	s_add_u32 s27, s27, s26
	s_mov_b32 s4, 0x4038aa3b
	s_mov_b32 s5, s4
	s_lshl_b32 s40, s26, 6
	s_waitcnt lgkmcnt(0)
	s_lshl_b32 s28, s24, 15
	s_add_u32 s28, s28, 0x1000
	s_add_u32 s10, s10, s28
	s_addc_u32 s11, s11, 0
	s_lshl_b32 s34, s41, 17
	s_lshl_b32 s35, s42, 9
	s_add_u32 s34, s34, s35
	s_add_u32 s34, s14, s34
	s_addc_u32 s35, s15, 0
	s_lshl_b32 s28, s27, 13
	s_add_u32 s28, s8, s28
	s_addc_u32 s29, s9, 0
	s_lshl_b32 s30, s27, 7
	s_add_u32 s30, s12, s30
	s_addc_u32 s31, s13, 0
	global_load_dwordx4 v[2:5], v156, s[10:11] offset:-4096
	global_load_dwordx4 v[6:9], v156, s[10:11] offset:0
	s_add_u32 s10, s10, 0x2000
	s_addc_u32 s11, s11, 0
	global_load_dwordx4 v[10:13], v156, s[10:11] offset:-4096
	global_load_dwordx4 v[14:17], v156, s[10:11] offset:0
	s_add_u32 s10, s10, 0x2000
	s_addc_u32 s11, s11, 0
	global_load_dwordx4 v[18:21], v156, s[10:11] offset:-4096
	global_load_dwordx4 v[22:25], v156, s[10:11] offset:0
	s_add_u32 s10, s10, 0x2000
	s_addc_u32 s11, s11, 0
	global_load_dwordx4 v[26:29], v156, s[10:11] offset:-4096
	global_load_dwordx4 v[30:33], v156, s[10:11] offset:0
	global_load_dwordx4 v[130:133], v160, s[34:35] offset:0
	global_load_dwordx4 v[134:137], v160, s[34:35] offset:128
	global_load_dwordx4 v[138:141], v160, s[34:35] offset:256
	global_load_dwordx4 v[142:145], v160, s[34:35] offset:384
	global_load_dwordx4 v[34:37], v158, s[28:29] offset:0
	global_load_dwordx4 v[38:41], v158, s[28:29] offset:16
	global_load_dwordx4 v[42:45], v158, s[28:29] offset:64
	global_load_dwordx4 v[46:49], v158, s[28:29] offset:80
	global_load_dwordx4 v[50:53], v158, s[28:29] offset:128
	global_load_dwordx4 v[54:57], v158, s[28:29] offset:144
	global_load_dwordx4 v[58:61], v158, s[28:29] offset:192
	global_load_dwordx4 v[62:65], v158, s[28:29] offset:208
	global_load_dwordx4 v[66:69], v159, s[30:31] offset:0
	global_load_dwordx4 v[70:73], v159, s[30:31] offset:32
	global_load_dwordx4 v[74:77], v159, s[30:31] offset:64
	global_load_dwordx4 v[78:81], v159, s[30:31] offset:96
	v_bfe_u32 v163, v0, 1, 3
	v_mul_u32_u24_e32 v163, 0x210, v163
	v_lshrrev_b32_e32 v164, 4, v0
	v_lshl_add_u32 v163, v164, 4, v163
	v_and_b32_e32 v164, 1, v0
	v_lshl_add_u32 v163, v164, 3, v163
	v_lshrrev_b32_e32 v164, 3, v0
	v_mul_u32_u24_e32 v164, 0x110, v164
	v_lshl_add_u32 v164, v161, 3, v164
	v_add_u32_e32 v164, 0x4200, v164
	v_mul_u32_u24_e32 v165, 0x210, v155
	v_lshl_add_u32 v165, v1, 4, v165
	v_mul_u32_u24_e32 v166, 0x110, v1
	v_lshl_add_u32 v166, v155, 4, v166
	v_add_u32_e32 v166, s40, v166
	v_add_u32_e32 v166, 0x4200, v166
	v_mul_u32_u24_e32 v167, 0x880, v155
	v_lshl_add_u32 v167, v1, 1, v167
	v_add_u32_e32 v167, s40, v167
	v_add_u32_e32 v167, 0x4200, v167
	s_lshl_b32 s32, s24, 18
	s_lshl_b32 s33, s27, 11
	s_add_u32 s32, s32, s33
	s_add_u32 s32, s16, s32
	s_addc_u32 s33, s17, 0
	s_lshl_b32 s36, s41, 16
	s_lshl_b32 s37, s42, 13
	s_add_u32 s36, s36, s37
	s_lshl_b32 s37, s26, 11
	s_add_u32 s36, s36, s37
	s_add_u32 s36, s20, s36
	s_addc_u32 s37, s21, 0
	s_lshl_b32 s38, s42, 18
	s_lshl_b32 s39, s26, 16
	s_add_u32 s38, s38, s39
	s_lshl_b32 s39, s41, 11
	s_add_u32 s38, s38, s39
	s_add_u32 s38, s22, s38
	s_addc_u32 s39, s23, 0
	s_waitcnt vmcnt(23)
	v_cvt_pk_f16_f32 v2, v2, v3
	v_cvt_pk_f16_f32 v3, v4, v5
	ds_write_b64 v163, v[2:3] offset:0
	s_waitcnt vmcnt(22)
	v_cvt_pk_f16_f32 v6, v6, v7
	v_cvt_pk_f16_f32 v7, v8, v9
	ds_write_b64 v163, v[6:7] offset:256
	s_waitcnt vmcnt(21)
	v_cvt_pk_f16_f32 v10, v10, v11
	v_cvt_pk_f16_f32 v11, v12, v13
	ds_write_b64 v163, v[10:11] offset:4224
	s_waitcnt vmcnt(20)
	v_cvt_pk_f16_f32 v14, v14, v15
	v_cvt_pk_f16_f32 v15, v16, v17
	ds_write_b64 v163, v[14:15] offset:4480
	s_waitcnt vmcnt(19)
	v_cvt_pk_f16_f32 v18, v18, v19
	v_cvt_pk_f16_f32 v19, v20, v21
	ds_write_b64 v163, v[18:19] offset:8448
	s_waitcnt vmcnt(18)
	v_cvt_pk_f16_f32 v22, v22, v23
	v_cvt_pk_f16_f32 v23, v24, v25
	ds_write_b64 v163, v[22:23] offset:8704
	s_waitcnt vmcnt(17)
	v_cvt_pk_f16_f32 v26, v26, v27
	v_cvt_pk_f16_f32 v27, v28, v29
	ds_write_b64 v163, v[26:27] offset:12672
	s_waitcnt vmcnt(16)
	v_cvt_pk_f16_f32 v30, v30, v31
	v_cvt_pk_f16_f32 v31, v32, v33
	ds_write_b64 v163, v[30:31] offset:12928
	s_waitcnt vmcnt(15)
	v_cvt_pk_f16_f32 v130, v130, v131
	v_cvt_pk_f16_f32 v131, v132, v133
	ds_write_b64 v164, v[130:131] offset:0
	s_waitcnt vmcnt(14)
	v_cvt_pk_f16_f32 v134, v134, v135
	v_cvt_pk_f16_f32 v135, v136, v137
	ds_write_b64 v164, v[134:135] offset:64
	s_waitcnt vmcnt(13)
	v_cvt_pk_f16_f32 v138, v138, v139
	v_cvt_pk_f16_f32 v139, v140, v141
	ds_write_b64 v164, v[138:139] offset:128
	s_waitcnt vmcnt(12)
	v_cvt_pk_f16_f32 v142, v142, v143
	v_cvt_pk_f16_f32 v143, v144, v145
	ds_write_b64 v164, v[142:143] offset:192
	s_waitcnt lgkmcnt(0)
	s_barrier
	ds_read_b128 v[130:133], v166
	ds_read_b128 v[134:137], v166 offset:32
	ds_read_u16 v138, v167 offset:0
	ds_read_u16 v139, v167 offset:272
	ds_read_u16 v140, v167 offset:544
	ds_read_u16 v141, v167 offset:816
	ds_read_u16 v142, v167 offset:1088
	ds_read_u16 v143, v167 offset:1360
	ds_read_u16 v144, v167 offset:1632
	ds_read_u16 v145, v167 offset:1904
	s_waitcnt vmcnt(4)
	v_cvt_pk_f16_f32 v82, v34, v35
	v_cvt_pk_f16_f32 v83, v36, v37
	v_cvt_pk_f16_f32 v84, v38, v39
	v_cvt_pk_f16_f32 v85, v40, v41
	v_cvt_pk_f16_f32 v86, v42, v43
	v_cvt_pk_f16_f32 v87, v44, v45
	v_cvt_pk_f16_f32 v88, v46, v47
	v_cvt_pk_f16_f32 v89, v48, v49
	v_cvt_pk_f16_f32 v90, v50, v51
	v_cvt_pk_f16_f32 v91, v52, v53
	v_cvt_pk_f16_f32 v92, v54, v55
	v_cvt_pk_f16_f32 v93, v56, v57
	v_cvt_pk_f16_f32 v94, v58, v59
	v_cvt_pk_f16_f32 v95, v60, v61
	v_cvt_pk_f16_f32 v96, v62, v63
	v_cvt_pk_f16_f32 v97, v64, v65
	s_waitcnt vmcnt(0)
	v_pk_mul_f32 v[66:67], v[66:67], s[4:5] op_sel_hi:[1,0]
	v_pk_mul_f32 v[68:69], v[68:69], s[4:5] op_sel_hi:[1,0]
	v_pk_mul_f32 v[70:71], v[70:71], s[4:5] op_sel_hi:[1,0]
	v_pk_mul_f32 v[72:73], v[72:73], s[4:5] op_sel_hi:[1,0]
	v_pk_mul_f32 v[74:75], v[74:75], s[4:5] op_sel_hi:[1,0]
	v_pk_mul_f32 v[76:77], v[76:77], s[4:5] op_sel_hi:[1,0]
	v_pk_mul_f32 v[78:79], v[78:79], s[4:5] op_sel_hi:[1,0]
	v_pk_mul_f32 v[80:81], v[80:81], s[4:5] op_sel_hi:[1,0]
	s_waitcnt lgkmcnt(8)
	global_store_dwordx4 v157, v[130:133], s[36:37] sc1
	global_store_dwordx4 v157, v[134:137], s[36:37] offset:1024 sc1
	s_waitcnt lgkmcnt(0)
	v_lshl_or_b32 v138, v139, 16, v138
	v_lshl_or_b32 v139, v141, 16, v140
	v_lshl_or_b32 v140, v143, 16, v142
	v_lshl_or_b32 v141, v145, 16, v144
	global_store_dwordx4 v157, v[138:141], s[38:39] sc1
	ds_read_u16 v142, v167 offset:4352
	ds_read_u16 v143, v167 offset:4624
	ds_read_u16 v144, v167 offset:4896
	ds_read_u16 v145, v167 offset:5168
	ds_read_u16 v146, v167 offset:5440
	ds_read_u16 v147, v167 offset:5712
	ds_read_u16 v148, v167 offset:5984
	ds_read_u16 v149, v167 offset:6256
	ds_read_b128 v[2:5], v165 offset:0
	ds_read_b128 v[6:9], v165 offset:1056
	ds_read_b128 v[10:13], v165 offset:2112
	ds_read_b128 v[14:17], v165 offset:3168
	s_waitcnt lgkmcnt(4)
	v_lshl_or_b32 v142, v143, 16, v142
	v_lshl_or_b32 v143, v145, 16, v144
	v_lshl_or_b32 v144, v147, 16, v146
	v_lshl_or_b32 v145, v149, 16, v148
	global_store_dwordx4 v157, v[142:145], s[38:39] offset:1024 sc1
	ds_read_b128 v[18:21], v165 offset:4224
	ds_read_b128 v[22:25], v165 offset:5280
	ds_read_b128 v[26:29], v165 offset:6336
	ds_read_b128 v[30:33], v165 offset:7392
	ds_read_b128 v[34:37], v165 offset:8448
	ds_read_b128 v[38:41], v165 offset:9504
	ds_read_b128 v[42:45], v165 offset:10560
	ds_read_b128 v[46:49], v165 offset:11616
	s_waitcnt lgkmcnt(8)
	v_mfma_f32_32x32x16_f16 v[98:113], v[82:85], v[2:5], 0
	v_mfma_f32_32x32x16_f16 v[98:113], v[86:89], v[6:9], v[98:113]
	v_mfma_f32_32x32x16_f16 v[98:113], v[90:93], v[10:13], v[98:113]
	v_mfma_f32_32x32x16_f16 v[98:113], v[94:97], v[14:17], v[98:113]
	ds_read_b128 v[50:53], v165 offset:12672
	ds_read_b128 v[54:57], v165 offset:13728
	ds_read_b128 v[58:61], v165 offset:14784
	ds_read_b128 v[62:65], v165 offset:15840
	s_waitcnt lgkmcnt(8)
	v_mfma_f32_32x32x16_f16 v[114:129], v[82:85], v[18:21], 0
	v_mfma_f32_32x32x16_f16 v[114:129], v[86:89], v[22:25], v[114:129]
	v_mfma_f32_32x32x16_f16 v[114:129], v[90:93], v[26:29], v[114:129]
	v_mfma_f32_32x32x16_f16 v[114:129], v[94:97], v[30:33], v[114:129]
	s_nop 7
	v_pk_fma_f32 v[130:131], v[98:99], s[4:5], v[66:67] op_sel_hi:[1,0,1]
	v_pk_fma_f32 v[132:133], v[100:101], s[4:5], v[68:69] op_sel_hi:[1,0,1]
	v_pk_fma_f32 v[134:135], v[102:103], s[4:5], v[70:71] op_sel_hi:[1,0,1]
	v_pk_fma_f32 v[136:137], v[104:105], s[4:5], v[72:73] op_sel_hi:[1,0,1]
	v_pk_fma_f32 v[138:139], v[106:107], s[4:5], v[74:75] op_sel_hi:[1,0,1]
	v_pk_fma_f32 v[140:141], v[108:109], s[4:5], v[76:77] op_sel_hi:[1,0,1]
	v_pk_fma_f32 v[142:143], v[110:111], s[4:5], v[78:79] op_sel_hi:[1,0,1]
	v_pk_fma_f32 v[144:145], v[112:113], s[4:5], v[80:81] op_sel_hi:[1,0,1]
	v_exp_f32_e32 v130, v130
	v_exp_f32_e32 v131, v131
	v_exp_f32_e32 v132, v132
	v_exp_f32_e32 v133, v133
	v_exp_f32_e32 v134, v134
	v_exp_f32_e32 v135, v135
	v_exp_f32_e32 v136, v136
	v_exp_f32_e32 v137, v137
	v_exp_f32_e32 v138, v138
	v_exp_f32_e32 v139, v139
	v_exp_f32_e32 v140, v140
	v_exp_f32_e32 v141, v141
	v_exp_f32_e32 v142, v142
	v_exp_f32_e32 v143, v143
	v_exp_f32_e32 v144, v144
	v_exp_f32_e32 v145, v145
	v_pk_add_f32 v[130:131], v[130:131], 1.0 op_sel_hi:[1,0]
	v_pk_add_f32 v[132:133], v[132:133], 1.0 op_sel_hi:[1,0]
	v_pk_add_f32 v[134:135], v[134:135], 1.0 op_sel_hi:[1,0]
	v_pk_add_f32 v[136:137], v[136:137], 1.0 op_sel_hi:[1,0]
	v_pk_add_f32 v[138:139], v[138:139], 1.0 op_sel_hi:[1,0]
	v_pk_add_f32 v[140:141], v[140:141], 1.0 op_sel_hi:[1,0]
	v_pk_add_f32 v[142:143], v[142:143], 1.0 op_sel_hi:[1,0]
	v_pk_add_f32 v[144:145], v[144:145], 1.0 op_sel_hi:[1,0]
	v_rcp_f32_e32 v130, v130
	v_rcp_f32_e32 v131, v131
	v_rcp_f32_e32 v132, v132
	v_rcp_f32_e32 v133, v133
	v_rcp_f32_e32 v134, v134
	v_rcp_f32_e32 v135, v135
	v_rcp_f32_e32 v136, v136
	v_rcp_f32_e32 v137, v137
	v_rcp_f32_e32 v138, v138
	v_rcp_f32_e32 v139, v139
	v_rcp_f32_e32 v140, v140
	v_rcp_f32_e32 v141, v141
	v_rcp_f32_e32 v142, v142
	v_rcp_f32_e32 v143, v143
	v_rcp_f32_e32 v144, v144
	v_rcp_f32_e32 v145, v145
	v_pk_fma_f32 v[130:131], v[130:131], 2.0, 1.0 op_sel_hi:[1,0,0] neg_lo:[1,0,0] neg_hi:[1,0,0]
	v_pk_fma_f32 v[132:133], v[132:133], 2.0, 1.0 op_sel_hi:[1,0,0] neg_lo:[1,0,0] neg_hi:[1,0,0]
	v_pk_fma_f32 v[134:135], v[134:135], 2.0, 1.0 op_sel_hi:[1,0,0] neg_lo:[1,0,0] neg_hi:[1,0,0]
	v_pk_fma_f32 v[136:137], v[136:137], 2.0, 1.0 op_sel_hi:[1,0,0] neg_lo:[1,0,0] neg_hi:[1,0,0]
	v_pk_fma_f32 v[138:139], v[138:139], 2.0, 1.0 op_sel_hi:[1,0,0] neg_lo:[1,0,0] neg_hi:[1,0,0]
	v_pk_fma_f32 v[140:141], v[140:141], 2.0, 1.0 op_sel_hi:[1,0,0] neg_lo:[1,0,0] neg_hi:[1,0,0]
	v_pk_fma_f32 v[142:143], v[142:143], 2.0, 1.0 op_sel_hi:[1,0,0] neg_lo:[1,0,0] neg_hi:[1,0,0]
	v_pk_fma_f32 v[144:145], v[144:145], 2.0, 1.0 op_sel_hi:[1,0,0] neg_lo:[1,0,0] neg_hi:[1,0,0]
	v_cvt_pk_f16_f32 v146, v130, v131
	v_cvt_pk_f16_f32 v147, v132, v133
	v_cvt_pk_f16_f32 v148, v134, v135
	v_cvt_pk_f16_f32 v149, v136, v137
	v_cvt_pk_f16_f32 v150, v138, v139
	v_cvt_pk_f16_f32 v151, v140, v141
	v_cvt_pk_f16_f32 v152, v142, v143
	v_cvt_pk_f16_f32 v153, v144, v145
	s_nop 1
	v_permlane32_swap_b32_e32 v146, v148
	v_permlane32_swap_b32_e32 v147, v149
	v_permlane32_swap_b32_e32 v150, v152
	v_permlane32_swap_b32_e32 v151, v153
	global_store_dwordx4 v157, v[146:149], s[32:33]
	global_store_dwordx4 v157, v[150:153], s[32:33] offset:1024
	s_add_u32 s32, s32, 0x10000
	s_addc_u32 s33, s33, 0
	s_waitcnt lgkmcnt(4)
	v_mfma_f32_32x32x16_f16 v[98:113], v[82:85], v[34:37], 0
	v_mfma_f32_32x32x16_f16 v[98:113], v[86:89], v[38:41], v[98:113]
	v_mfma_f32_32x32x16_f16 v[98:113], v[90:93], v[42:45], v[98:113]
	v_mfma_f32_32x32x16_f16 v[98:113], v[94:97], v[46:49], v[98:113]
	v_pk_fma_f32 v[130:131], v[114:115], s[4:5], v[66:67] op_sel_hi:[1,0,1]
	v_pk_fma_f32 v[132:133], v[116:117], s[4:5], v[68:69] op_sel_hi:[1,0,1]
	v_pk_fma_f32 v[134:135], v[118:119], s[4:5], v[70:71] op_sel_hi:[1,0,1]
	v_pk_fma_f32 v[136:137], v[120:121], s[4:5], v[72:73] op_sel_hi:[1,0,1]
	v_pk_fma_f32 v[138:139], v[122:123], s[4:5], v[74:75] op_sel_hi:[1,0,1]
	v_pk_fma_f32 v[140:141], v[124:125], s[4:5], v[76:77] op_sel_hi:[1,0,1]
	v_pk_fma_f32 v[142:143], v[126:127], s[4:5], v[78:79] op_sel_hi:[1,0,1]
	v_pk_fma_f32 v[144:145], v[128:129], s[4:5], v[80:81] op_sel_hi:[1,0,1]
	v_exp_f32_e32 v130, v130
	v_exp_f32_e32 v131, v131
	v_exp_f32_e32 v132, v132
	v_exp_f32_e32 v133, v133
	v_exp_f32_e32 v134, v134
	v_exp_f32_e32 v135, v135
	v_exp_f32_e32 v136, v136
	v_exp_f32_e32 v137, v137
	v_exp_f32_e32 v138, v138
	v_exp_f32_e32 v139, v139
	v_exp_f32_e32 v140, v140
	v_exp_f32_e32 v141, v141
	v_exp_f32_e32 v142, v142
	v_exp_f32_e32 v143, v143
	v_exp_f32_e32 v144, v144
	v_exp_f32_e32 v145, v145
	v_pk_add_f32 v[130:131], v[130:131], 1.0 op_sel_hi:[1,0]
	v_pk_add_f32 v[132:133], v[132:133], 1.0 op_sel_hi:[1,0]
	v_pk_add_f32 v[134:135], v[134:135], 1.0 op_sel_hi:[1,0]
	v_pk_add_f32 v[136:137], v[136:137], 1.0 op_sel_hi:[1,0]
	v_pk_add_f32 v[138:139], v[138:139], 1.0 op_sel_hi:[1,0]
	v_pk_add_f32 v[140:141], v[140:141], 1.0 op_sel_hi:[1,0]
	v_pk_add_f32 v[142:143], v[142:143], 1.0 op_sel_hi:[1,0]
	v_pk_add_f32 v[144:145], v[144:145], 1.0 op_sel_hi:[1,0]
	v_rcp_f32_e32 v130, v130
	v_rcp_f32_e32 v131, v131
	v_rcp_f32_e32 v132, v132
	v_rcp_f32_e32 v133, v133
	v_rcp_f32_e32 v134, v134
	v_rcp_f32_e32 v135, v135
	v_rcp_f32_e32 v136, v136
	v_rcp_f32_e32 v137, v137
	v_rcp_f32_e32 v138, v138
	v_rcp_f32_e32 v139, v139
	v_rcp_f32_e32 v140, v140
	v_rcp_f32_e32 v141, v141
	v_rcp_f32_e32 v142, v142
	v_rcp_f32_e32 v143, v143
	v_rcp_f32_e32 v144, v144
	v_rcp_f32_e32 v145, v145
	v_pk_fma_f32 v[130:131], v[130:131], 2.0, 1.0 op_sel_hi:[1,0,0] neg_lo:[1,0,0] neg_hi:[1,0,0]
	v_pk_fma_f32 v[132:133], v[132:133], 2.0, 1.0 op_sel_hi:[1,0,0] neg_lo:[1,0,0] neg_hi:[1,0,0]
	v_pk_fma_f32 v[134:135], v[134:135], 2.0, 1.0 op_sel_hi:[1,0,0] neg_lo:[1,0,0] neg_hi:[1,0,0]
	v_pk_fma_f32 v[136:137], v[136:137], 2.0, 1.0 op_sel_hi:[1,0,0] neg_lo:[1,0,0] neg_hi:[1,0,0]
	v_pk_fma_f32 v[138:139], v[138:139], 2.0, 1.0 op_sel_hi:[1,0,0] neg_lo:[1,0,0] neg_hi:[1,0,0]
	v_pk_fma_f32 v[140:141], v[140:141], 2.0, 1.0 op_sel_hi:[1,0,0] neg_lo:[1,0,0] neg_hi:[1,0,0]
	v_pk_fma_f32 v[142:143], v[142:143], 2.0, 1.0 op_sel_hi:[1,0,0] neg_lo:[1,0,0] neg_hi:[1,0,0]
	v_pk_fma_f32 v[144:145], v[144:145], 2.0, 1.0 op_sel_hi:[1,0,0] neg_lo:[1,0,0] neg_hi:[1,0,0]
	v_cvt_pk_f16_f32 v146, v130, v131
	v_cvt_pk_f16_f32 v147, v132, v133
	v_cvt_pk_f16_f32 v148, v134, v135
	v_cvt_pk_f16_f32 v149, v136, v137
	v_cvt_pk_f16_f32 v150, v138, v139
	v_cvt_pk_f16_f32 v151, v140, v141
	v_cvt_pk_f16_f32 v152, v142, v143
	v_cvt_pk_f16_f32 v153, v144, v145
	s_nop 1
	v_permlane32_swap_b32_e32 v146, v148
	v_permlane32_swap_b32_e32 v147, v149
	v_permlane32_swap_b32_e32 v150, v152
	v_permlane32_swap_b32_e32 v151, v153
	global_store_dwordx4 v157, v[146:149], s[32:33]
	global_store_dwordx4 v157, v[150:153], s[32:33] offset:1024
	s_add_u32 s32, s32, 0x10000
	s_addc_u32 s33, s33, 0
	s_waitcnt lgkmcnt(0)
	v_mfma_f32_32x32x16_f16 v[114:129], v[82:85], v[50:53], 0
	v_mfma_f32_32x32x16_f16 v[114:129], v[86:89], v[54:57], v[114:129]
	v_mfma_f32_32x32x16_f16 v[114:129], v[90:93], v[58:61], v[114:129]
	v_mfma_f32_32x32x16_f16 v[114:129], v[94:97], v[62:65], v[114:129]
	v_pk_fma_f32 v[130:131], v[98:99], s[4:5], v[66:67] op_sel_hi:[1,0,1]
	v_pk_fma_f32 v[132:133], v[100:101], s[4:5], v[68:69] op_sel_hi:[1,0,1]
	v_pk_fma_f32 v[134:135], v[102:103], s[4:5], v[70:71] op_sel_hi:[1,0,1]
	v_pk_fma_f32 v[136:137], v[104:105], s[4:5], v[72:73] op_sel_hi:[1,0,1]
	v_pk_fma_f32 v[138:139], v[106:107], s[4:5], v[74:75] op_sel_hi:[1,0,1]
	v_pk_fma_f32 v[140:141], v[108:109], s[4:5], v[76:77] op_sel_hi:[1,0,1]
	v_pk_fma_f32 v[142:143], v[110:111], s[4:5], v[78:79] op_sel_hi:[1,0,1]
	v_pk_fma_f32 v[144:145], v[112:113], s[4:5], v[80:81] op_sel_hi:[1,0,1]
	v_exp_f32_e32 v130, v130
	v_exp_f32_e32 v131, v131
	v_exp_f32_e32 v132, v132
	v_exp_f32_e32 v133, v133
	v_exp_f32_e32 v134, v134
	v_exp_f32_e32 v135, v135
	v_exp_f32_e32 v136, v136
	v_exp_f32_e32 v137, v137
	v_exp_f32_e32 v138, v138
	v_exp_f32_e32 v139, v139
	v_exp_f32_e32 v140, v140
	v_exp_f32_e32 v141, v141
	v_exp_f32_e32 v142, v142
	v_exp_f32_e32 v143, v143
	v_exp_f32_e32 v144, v144
	v_exp_f32_e32 v145, v145
	v_pk_add_f32 v[130:131], v[130:131], 1.0 op_sel_hi:[1,0]
	v_pk_add_f32 v[132:133], v[132:133], 1.0 op_sel_hi:[1,0]
	v_pk_add_f32 v[134:135], v[134:135], 1.0 op_sel_hi:[1,0]
	v_pk_add_f32 v[136:137], v[136:137], 1.0 op_sel_hi:[1,0]
	v_pk_add_f32 v[138:139], v[138:139], 1.0 op_sel_hi:[1,0]
	v_pk_add_f32 v[140:141], v[140:141], 1.0 op_sel_hi:[1,0]
	v_pk_add_f32 v[142:143], v[142:143], 1.0 op_sel_hi:[1,0]
	v_pk_add_f32 v[144:145], v[144:145], 1.0 op_sel_hi:[1,0]
	v_rcp_f32_e32 v130, v130
	v_rcp_f32_e32 v131, v131
	v_rcp_f32_e32 v132, v132
	v_rcp_f32_e32 v133, v133
	v_rcp_f32_e32 v134, v134
	v_rcp_f32_e32 v135, v135
	v_rcp_f32_e32 v136, v136
	v_rcp_f32_e32 v137, v137
	v_rcp_f32_e32 v138, v138
	v_rcp_f32_e32 v139, v139
	v_rcp_f32_e32 v140, v140
	v_rcp_f32_e32 v141, v141
	v_rcp_f32_e32 v142, v142
	v_rcp_f32_e32 v143, v143
	v_rcp_f32_e32 v144, v144
	v_rcp_f32_e32 v145, v145
	v_pk_fma_f32 v[130:131], v[130:131], 2.0, 1.0 op_sel_hi:[1,0,0] neg_lo:[1,0,0] neg_hi:[1,0,0]
	v_pk_fma_f32 v[132:133], v[132:133], 2.0, 1.0 op_sel_hi:[1,0,0] neg_lo:[1,0,0] neg_hi:[1,0,0]
	v_pk_fma_f32 v[134:135], v[134:135], 2.0, 1.0 op_sel_hi:[1,0,0] neg_lo:[1,0,0] neg_hi:[1,0,0]
	v_pk_fma_f32 v[136:137], v[136:137], 2.0, 1.0 op_sel_hi:[1,0,0] neg_lo:[1,0,0] neg_hi:[1,0,0]
	v_pk_fma_f32 v[138:139], v[138:139], 2.0, 1.0 op_sel_hi:[1,0,0] neg_lo:[1,0,0] neg_hi:[1,0,0]
	v_pk_fma_f32 v[140:141], v[140:141], 2.0, 1.0 op_sel_hi:[1,0,0] neg_lo:[1,0,0] neg_hi:[1,0,0]
	v_pk_fma_f32 v[142:143], v[142:143], 2.0, 1.0 op_sel_hi:[1,0,0] neg_lo:[1,0,0] neg_hi:[1,0,0]
	v_pk_fma_f32 v[144:145], v[144:145], 2.0, 1.0 op_sel_hi:[1,0,0] neg_lo:[1,0,0] neg_hi:[1,0,0]
	v_cvt_pk_f16_f32 v146, v130, v131
	v_cvt_pk_f16_f32 v147, v132, v133
	v_cvt_pk_f16_f32 v148, v134, v135
	v_cvt_pk_f16_f32 v149, v136, v137
	v_cvt_pk_f16_f32 v150, v138, v139
	v_cvt_pk_f16_f32 v151, v140, v141
	v_cvt_pk_f16_f32 v152, v142, v143
	v_cvt_pk_f16_f32 v153, v144, v145
	s_nop 1
	v_permlane32_swap_b32_e32 v146, v148
	v_permlane32_swap_b32_e32 v147, v149
	v_permlane32_swap_b32_e32 v150, v152
	v_permlane32_swap_b32_e32 v151, v153
	global_store_dwordx4 v157, v[146:149], s[32:33]
	global_store_dwordx4 v157, v[150:153], s[32:33] offset:1024
	s_add_u32 s32, s32, 0x10000
	s_addc_u32 s33, s33, 0
	s_nop 7
	v_pk_fma_f32 v[130:131], v[114:115], s[4:5], v[66:67] op_sel_hi:[1,0,1]
	v_pk_fma_f32 v[132:133], v[116:117], s[4:5], v[68:69] op_sel_hi:[1,0,1]
	v_pk_fma_f32 v[134:135], v[118:119], s[4:5], v[70:71] op_sel_hi:[1,0,1]
	v_pk_fma_f32 v[136:137], v[120:121], s[4:5], v[72:73] op_sel_hi:[1,0,1]
	v_pk_fma_f32 v[138:139], v[122:123], s[4:5], v[74:75] op_sel_hi:[1,0,1]
	v_pk_fma_f32 v[140:141], v[124:125], s[4:5], v[76:77] op_sel_hi:[1,0,1]
	v_pk_fma_f32 v[142:143], v[126:127], s[4:5], v[78:79] op_sel_hi:[1,0,1]
	v_pk_fma_f32 v[144:145], v[128:129], s[4:5], v[80:81] op_sel_hi:[1,0,1]
	v_exp_f32_e32 v130, v130
	v_exp_f32_e32 v131, v131
	v_exp_f32_e32 v132, v132
	v_exp_f32_e32 v133, v133
	v_exp_f32_e32 v134, v134
	v_exp_f32_e32 v135, v135
	v_exp_f32_e32 v136, v136
	v_exp_f32_e32 v137, v137
	v_exp_f32_e32 v138, v138
	v_exp_f32_e32 v139, v139
	v_exp_f32_e32 v140, v140
	v_exp_f32_e32 v141, v141
	v_exp_f32_e32 v142, v142
	v_exp_f32_e32 v143, v143
	v_exp_f32_e32 v144, v144
	v_exp_f32_e32 v145, v145
	v_pk_add_f32 v[130:131], v[130:131], 1.0 op_sel_hi:[1,0]
	v_pk_add_f32 v[132:133], v[132:133], 1.0 op_sel_hi:[1,0]
	v_pk_add_f32 v[134:135], v[134:135], 1.0 op_sel_hi:[1,0]
	v_pk_add_f32 v[136:137], v[136:137], 1.0 op_sel_hi:[1,0]
	v_pk_add_f32 v[138:139], v[138:139], 1.0 op_sel_hi:[1,0]
	v_pk_add_f32 v[140:141], v[140:141], 1.0 op_sel_hi:[1,0]
	v_pk_add_f32 v[142:143], v[142:143], 1.0 op_sel_hi:[1,0]
	v_pk_add_f32 v[144:145], v[144:145], 1.0 op_sel_hi:[1,0]
	v_rcp_f32_e32 v130, v130
	v_rcp_f32_e32 v131, v131
	v_rcp_f32_e32 v132, v132
	v_rcp_f32_e32 v133, v133
	v_rcp_f32_e32 v134, v134
	v_rcp_f32_e32 v135, v135
	v_rcp_f32_e32 v136, v136
	v_rcp_f32_e32 v137, v137
	v_rcp_f32_e32 v138, v138
	v_rcp_f32_e32 v139, v139
	v_rcp_f32_e32 v140, v140
	v_rcp_f32_e32 v141, v141
	v_rcp_f32_e32 v142, v142
	v_rcp_f32_e32 v143, v143
	v_rcp_f32_e32 v144, v144
	v_rcp_f32_e32 v145, v145
	v_pk_fma_f32 v[130:131], v[130:131], 2.0, 1.0 op_sel_hi:[1,0,0] neg_lo:[1,0,0] neg_hi:[1,0,0]
	v_pk_fma_f32 v[132:133], v[132:133], 2.0, 1.0 op_sel_hi:[1,0,0] neg_lo:[1,0,0] neg_hi:[1,0,0]
	v_pk_fma_f32 v[134:135], v[134:135], 2.0, 1.0 op_sel_hi:[1,0,0] neg_lo:[1,0,0] neg_hi:[1,0,0]
	v_pk_fma_f32 v[136:137], v[136:137], 2.0, 1.0 op_sel_hi:[1,0,0] neg_lo:[1,0,0] neg_hi:[1,0,0]
	v_pk_fma_f32 v[138:139], v[138:139], 2.0, 1.0 op_sel_hi:[1,0,0] neg_lo:[1,0,0] neg_hi:[1,0,0]
	v_pk_fma_f32 v[140:141], v[140:141], 2.0, 1.0 op_sel_hi:[1,0,0] neg_lo:[1,0,0] neg_hi:[1,0,0]
	v_pk_fma_f32 v[142:143], v[142:143], 2.0, 1.0 op_sel_hi:[1,0,0] neg_lo:[1,0,0] neg_hi:[1,0,0]
	v_pk_fma_f32 v[144:145], v[144:145], 2.0, 1.0 op_sel_hi:[1,0,0] neg_lo:[1,0,0] neg_hi:[1,0,0]
	v_cvt_pk_f16_f32 v146, v130, v131
	v_cvt_pk_f16_f32 v147, v132, v133
	v_cvt_pk_f16_f32 v148, v134, v135
	v_cvt_pk_f16_f32 v149, v136, v137
	v_cvt_pk_f16_f32 v150, v138, v139
	v_cvt_pk_f16_f32 v151, v140, v141
	v_cvt_pk_f16_f32 v152, v142, v143
	v_cvt_pk_f16_f32 v153, v144, v145
	s_nop 1
	v_permlane32_swap_b32_e32 v146, v148
	v_permlane32_swap_b32_e32 v147, v149
	v_permlane32_swap_b32_e32 v150, v152
	v_permlane32_swap_b32_e32 v151, v153
	global_store_dwordx4 v157, v[146:149], s[32:33]
	global_store_dwordx4 v157, v[150:153], s[32:33] offset:1024
	s_endpgm
